# v34 + P9 final stage: the 14 ln2_w/ln2_b slice loads hoisted above the wave reductions into dead registers; per-step load,load,vmcnt(0) ladder replaced by counted vmcnt(14-j) so output-store acks are
# speedup vs baseline: 1.0022x; 1.0022x over previous
; __device__ __forceinline__ float bf_lo(unsigned w) { return __uint_as_float(w << 16); }
; __device__ __forceinline__ float bf_hi(unsigned w) { return __uint_as_float(w & 0xffff0000u); }
; __device__ __forceinline__ void p9_final(Frame& F) {
;     ...
;     for (int t = gw; t < NTOK; t += NGW) {
;         const int b = t >> 12;
;         const i32x4 ae = ae_n, ap = ap_n; const f32x4 aw = aw_n;
;         { const int tn = (t + NGW < NTOK) ? t + NGW : t;
;           ae_n = ((const i32x4*)(F.ws + WS_ASG_E))[tn]; ap_n = ((const i32x4*)(F.ws + WS_ASG_P))[tn]; aw_n = ((const f32x4*)(F.ws + WS_ASG_W))[tn]; }
;         const u32x2* yr[4];
; #pragma unroll
;         for (int k = 0; k < 4; ++k) yr[k] = (const u32x2*)(Y + ((size_t)tab[352 + ae[k]] * 256 + ap[k]) * DM) + lane;
;         u32x2 q[4][8]; f32x4 x1[8];
; #pragma unroll
;         for (int k = 0; k < 4; ++k)
; #pragma unroll
;             for (int j = 0; j < 8; ++j) q[k][j] = yr[k][64 * j];
; #pragma unroll
;         for (int j = 0; j < 8; ++j) { const u32x2 xb = ((const u32x2*)(X1 + (size_t)t * DM))[lane + 64 * j]; x1[j] = (f32x4){bf_lo(xb.x), bf_hi(xb.x), bf_lo(xb.y), bf_hi(xb.y)}; }
.LBB0_1211:
	global_load_dwordx2 v[50:51], v[48:49], off
	global_load_dwordx2 v[52:53], v[48:49], off offset:512
	global_load_dwordx2 v[54:55], v[48:49], off offset:1024
	global_load_dwordx2 v[56:57], v[48:49], off offset:1536
	global_load_dwordx2 v[58:59], v[48:49], off offset:2048
	global_load_dwordx2 v[60:61], v[48:49], off offset:2560
	global_load_dwordx2 v[62:63], v[48:49], off offset:3072
	global_load_dwordx2 v[64:65], v[48:49], off offset:3584
	s_add_i32 s28, s14, s4
	s_cmpk_lt_i32 s28, 0x2000
	s_cselect_b64 s[24:25], -1, 0
	v_lshlrev_b32_e32 v4, 2, v4
	v_lshlrev_b32_e32 v6, 2, v6
	s_and_b64 s[30:31], s[24:25], exec
	v_lshlrev_b32_e32 v5, 2, v5
	v_lshlrev_b32_e32 v7, 2, v7
	v_add_u32_e32 v4, s5, v4
	v_add_u32_e32 v8, s5, v6
	s_cselect_b32 s30, s28, s14
	global_load_dwordx4 v[16:19], v[26:27], off
	global_load_dwordx4 v[20:23], v[28:29], off
	v_add_u32_e32 v5, s5, v5
	v_add_u32_e32 v7, s5, v7
	ds_read_b32 v4, v4
	ds_read_b32 v6, v5
	ds_read_b32 v8, v8
	ds_read_b32 v10, v7
	s_ashr_i32 s31, s30, 31
	s_lshl_b64 s[30:31], s[30:31], 4
	s_add_u32 s36, s34, s30
	s_waitcnt lgkmcnt(3)
	v_ashrrev_i32_e32 v5, 31, v4
	s_waitcnt lgkmcnt(2)
	v_ashrrev_i32_e32 v7, 31, v6
	s_addc_u32 s37, s35, s31
	v_lshlrev_b64 v[12:13], 20, v[4:5]
	v_lshlrev_b64 v[14:15], 20, v[6:7]
	global_load_dwordx4 v[4:7], v25, s[36:37]
	s_add_u32 s36, s27, s30
	s_addc_u32 s37, s33, s31
	s_add_u32 s30, s13, s30
	s_mov_b32 s16, s0
	s_waitcnt lgkmcnt(1)
	v_ashrrev_i32_e32 v9, 31, v8
	s_waitcnt lgkmcnt(0)
	v_ashrrev_i32_e32 v11, 31, v10
	s_addc_u32 s31, s26, s31
	s_ashr_i32 s17, s0, 31
	s_mov_b32 s18, s1
	s_mov_b32 s20, s2
	s_mov_b32 s22, s3
	v_lshlrev_b64 v[8:9], 20, v[8:9]
	v_lshlrev_b64 v[10:11], 20, v[10:11]
	v_lshl_add_u64 v[84:85], s[6:7], 0, v[12:13]
	s_ashr_i32 s19, s1, 31
	s_ashr_i32 s21, s2, 31
	s_ashr_i32 s23, s3, 31
	s_lshl_b64 s[0:1], s[16:17], 12
	v_lshl_add_u64 v[86:87], s[6:7], 0, v[14:15]
	v_lshl_add_u64 v[88:89], s[6:7], 0, v[8:9]
	v_lshl_add_u64 v[90:91], s[6:7], 0, v[10:11]
	s_lshl_b64 s[2:3], s[18:19], 12
	s_lshl_b64 s[16:17], s[20:21], 12
	s_lshl_b64 s[18:19], s[22:23], 12
	v_lshl_add_u64 v[84:85], v[84:85], 0, s[0:1]
	v_lshlrev_b32_e32 v81, 3, v170
	v_lshl_add_u64 v[86:87], v[86:87], 0, s[2:3]
	v_lshl_add_u64 v[88:89], v[88:89], 0, s[16:17]
	v_lshl_add_u64 v[90:91], v[90:91], 0, s[18:19]
	v_readfirstlane_b32 s0, v84
	v_readfirstlane_b32 s1, v85
	global_load_dwordx4 v[8:11], v25, s[36:37]
	global_load_dwordx4 v[12:15], v25, s[30:31]
	v_readfirstlane_b32 s2, v86
	v_readfirstlane_b32 s3, v87
	v_readfirstlane_b32 s16, v88
	v_readfirstlane_b32 s17, v89
	v_readfirstlane_b32 s18, v90
	v_readfirstlane_b32 s19, v91
	global_load_dwordx2 v[102:103], v81, s[0:1]
	global_load_dwordx2 v[104:105], v81, s[2:3]
	s_nop 0
	global_load_dwordx2 v[106:107], v81, s[16:17]
	s_nop 0
	global_load_dwordx2 v[108:109], v81, s[18:19]
	global_load_dwordx2 v[110:111], v81, s[0:1] offset:512
	global_load_dwordx2 v[112:113], v81, s[0:1] offset:1024
	global_load_dwordx2 v[114:115], v81, s[0:1] offset:1536
	global_load_dwordx2 v[116:117], v81, s[2:3] offset:512
	global_load_dwordx2 v[118:119], v81, s[16:17] offset:512
	global_load_dwordx2 v[120:121], v81, s[0:1] offset:2048
	global_load_dwordx2 v[122:123], v81, s[0:1] offset:2560
	global_load_dwordx2 v[124:125], v81, s[0:1] offset:3072
	global_load_dwordx2 v[126:127], v81, s[0:1] offset:3584
	global_load_dwordx2 v[128:129], v81, s[18:19] offset:512
	global_load_dwordx2 v[130:131], v81, s[2:3] offset:1024
	global_load_dwordx2 v[132:133], v81, s[2:3] offset:1536
	global_load_dwordx2 v[134:135], v81, s[2:3] offset:2048
	global_load_dwordx2 v[136:137], v81, s[2:3] offset:2560
	global_load_dwordx2 v[138:139], v81, s[2:3] offset:3072
	global_load_dwordx2 v[140:141], v81, s[2:3] offset:3584
	global_load_dwordx2 v[142:143], v81, s[16:17] offset:1024
	global_load_dwordx2 v[144:145], v81, s[16:17] offset:1536
	global_load_dwordx2 v[146:147], v81, s[16:17] offset:2048
	global_load_dwordx2 v[148:149], v81, s[16:17] offset:2560
	global_load_dwordx2 v[150:151], v81, s[16:17] offset:3072
	global_load_dwordx2 v[152:153], v81, s[16:17] offset:3584
	global_load_dwordx2 v[154:155], v81, s[18:19] offset:1024
	global_load_dwordx2 v[156:157], v81, s[18:19] offset:1536
	global_load_dwordx2 v[158:159], v81, s[18:19] offset:2048
	global_load_dwordx2 v[160:161], v81, s[18:19] offset:2560
	global_load_dwordx2 v[162:163], v81, s[18:19] offset:3072
	global_load_dwordx2 v[164:165], v81, s[18:19] offset:3584
	s_ashr_i32 s14, s14, 12
	s_mul_hi_i32 s20, s14, 0xc000
	s_mul_i32 s14, s14, 0xc000
	s_add_u32 s14, s82, s14
	s_addc_u32 s20, s83, s20
	s_add_u32 s0, s14, 0x10a000
	v_lshlrev_b32_e32 v82, 4, v170
	s_addc_u32 s1, s20, 0
	s_waitcnt vmcnt(44)
	v_lshlrev_b32_e32 v166, 16, v50
	v_and_b32_e32 v167, 0xffff0000, v50
	v_lshlrev_b32_e32 v168, 16, v51
	v_and_b32_e32 v169, 0xffff0000, v51
	s_waitcnt vmcnt(40)
	v_lshlrev_b32_e32 v184, 16, v58
	v_and_b32_e32 v185, 0xffff0000, v58
	v_lshlrev_b32_e32 v186, 16, v59
	v_and_b32_e32 v187, 0xffff0000, v59
	v_lshlrev_b32_e32 v176, 16, v54
	v_and_b32_e32 v177, 0xffff0000, v54
	v_lshlrev_b32_e32 v178, 16, v55
	v_and_b32_e32 v179, 0xffff0000, v55
	s_waitcnt vmcnt(39)
	v_lshlrev_b32_e32 v188, 16, v60
	v_and_b32_e32 v189, 0xffff0000, v60
	v_lshlrev_b32_e32 v190, 16, v61
	v_and_b32_e32 v191, 0xffff0000, v61
	v_lshlrev_b32_e32 v172, 16, v52
	v_and_b32_e32 v173, 0xffff0000, v52
	v_lshlrev_b32_e32 v174, 16, v53
	v_and_b32_e32 v175, 0xffff0000, v53
	v_lshlrev_b32_e32 v180, 16, v56
	v_and_b32_e32 v181, 0xffff0000, v56
	v_lshlrev_b32_e32 v182, 16, v57
	v_and_b32_e32 v183, 0xffff0000, v57
	global_load_dwordx4 v[82:85], v82, s[0:1]
	s_nop 0
	global_load_dwordx4 v[86:89], v72, s[0:1]
	global_load_dwordx4 v[90:93], v73, s[0:1]
	global_load_dwordx4 v[94:97], v74, s[0:1]
	global_load_dwordx4 v[98:101], v75, s[0:1]
	v_mov_b32_e32 v24, v3
	s_waitcnt vmcnt(43)
; __device__ __forceinline__ float bf_lo(unsigned w) { return __uint_as_float(w << 16); }
; __device__ __forceinline__ float bf_hi(unsigned w) { return __uint_as_float(w & 0xffff0000u); }
; __device__ __forceinline__ void p9_final(Frame& F) {
;     ...
;         for (int j = 0; j < 8; ++j) { const u32x2 xb = ((const u32x2*)(X1 + (size_t)t * DM))[lane + 64 * j]; x1[j] = (f32x4){bf_lo(xb.x), bf_hi(xb.x), bf_lo(xb.y), bf_hi(xb.y)}; }
;         float s = 0.f; f32x4 v[8];
; #pragma unroll
;         for (int j = 0; j < 8; ++j) { f32x4 y = {0.f, 0.f, 0.f, 0.f};
; #pragma unroll
;             for (int k = 0; k < 4; ++k) { const float w = aw[k]; y[0] += w * bf_lo(q[k][j].x); y[1] += w * bf_hi(q[k][j].x); y[2] += w * bf_lo(q[k][j].y); y[3] += w * bf_hi(q[k][j].y); }
;             v[j] = x1[j] * DN_ALPHA + ((const f32x4*)(mod + (size_t)b * 12288 + 10240))[lane + 64 * j] * y; s += (v[j][0] + v[j][1]) + (v[j][2] + v[j][3]); }
	v_lshlrev_b32_e32 v192, 16, v62
	v_and_b32_e32 v193, 0xffff0000, v62
	v_lshlrev_b32_e32 v62, 16, v63
	v_and_b32_e32 v63, 0xffff0000, v63
	s_waitcnt vmcnt(42)
	v_lshlrev_b32_e32 v194, 16, v64
	v_and_b32_e32 v195, 0xffff0000, v64
	v_lshlrev_b32_e32 v64, 16, v65
	v_and_b32_e32 v65, 0xffff0000, v65
	v_lshl_add_u64 v[48:49], v[48:49], 0, s[10:11]
	s_mov_b32 s14, s28
	s_waitcnt vmcnt(36)
	v_lshlrev_b32_e32 v50, 16, v102
	v_and_b32_e32 v51, 0xffff0000, v102
	v_lshlrev_b32_e32 v54, 16, v103
	v_and_b32_e32 v55, 0xffff0000, v103
	s_waitcnt vmcnt(32)
	v_lshlrev_b32_e32 v58, 16, v110
	v_and_b32_e32 v59, 0xffff0000, v110
	v_lshlrev_b32_e32 v110, 16, v111
	s_waitcnt vmcnt(29)
	v_lshlrev_b32_e32 v60, 16, v116
	v_and_b32_e32 v61, 0xffff0000, v116
	v_and_b32_e32 v111, 0xffff0000, v111
	v_lshlrev_b32_e32 v200, 16, v112
	v_and_b32_e32 v201, 0xffff0000, v112
	v_pk_fma_f32 v[58:59], v[0:1], v[58:59], 0 op_sel_hi:[0,1,0]
	v_lshlrev_b32_e32 v52, 16, v104
	v_and_b32_e32 v53, 0xffff0000, v104
	v_lshlrev_b32_e32 v56, 16, v105
	v_and_b32_e32 v57, 0xffff0000, v105
	v_lshlrev_b32_e32 v116, 16, v117
	v_and_b32_e32 v117, 0xffff0000, v117
	s_waitcnt vmcnt(22)
	v_lshlrev_b32_e32 v202, 16, v130
	v_and_b32_e32 v203, 0xffff0000, v130
	v_pk_fma_f32 v[50:51], v[0:1], v[50:51], 0 op_sel_hi:[0,1,0]
	v_pk_fma_f32 v[54:55], v[0:1], v[54:55], 0 op_sel_hi:[0,1,0]
	v_pk_fma_f32 v[252:253], v[0:1], v[60:61], v[58:59] op_sel:[1,0,0]
	v_pk_fma_f32 v[58:59], v[0:1], v[110:111], 0 op_sel_hi:[0,1,0]
	v_pk_fma_f32 v[60:61], v[0:1], v[200:201], 0 op_sel_hi:[0,1,0]
	v_pk_fma_f32 v[248:249], v[0:1], v[52:53], v[50:51] op_sel:[1,0,0]
	global_load_dwordx4 v[50:53], v76, s[0:1]
	v_pk_fma_f32 v[250:251], v[0:1], v[56:57], v[54:55] op_sel:[1,0,0]
	global_load_dwordx4 v[54:57], v77, s[0:1]
	v_pk_fma_f32 v[110:111], v[0:1], v[116:117], v[58:59] op_sel:[1,0,0]
	v_pk_fma_f32 v[116:117], v[0:1], v[202:203], v[60:61] op_sel:[1,0,0]
	global_load_dwordx4 v[58:61], v78, s[0:1]
	v_lshlrev_b32_e32 v112, 16, v113
	v_and_b32_e32 v113, 0xffff0000, v113
	v_lshlrev_b32_e32 v208, 16, v114
	v_and_b32_e32 v209, 0xffff0000, v114
	v_lshlrev_b32_e32 v114, 16, v115
	v_and_b32_e32 v115, 0xffff0000, v115
	v_lshlrev_b32_e32 v216, 16, v120
	v_and_b32_e32 v217, 0xffff0000, v120
	v_lshlrev_b32_e32 v120, 16, v121
	v_and_b32_e32 v121, 0xffff0000, v121
	v_lshlrev_b32_e32 v224, 16, v122
	v_and_b32_e32 v225, 0xffff0000, v122
	v_lshlrev_b32_e32 v122, 16, v123
	v_and_b32_e32 v123, 0xffff0000, v123
	v_lshlrev_b32_e32 v232, 16, v124
	v_and_b32_e32 v233, 0xffff0000, v124
	v_lshlrev_b32_e32 v124, 16, v125
	v_and_b32_e32 v125, 0xffff0000, v125
	v_lshlrev_b32_e32 v240, 16, v126
	v_and_b32_e32 v241, 0xffff0000, v126
	v_lshlrev_b32_e32 v126, 16, v127
	v_and_b32_e32 v127, 0xffff0000, v127
	v_lshlrev_b32_e32 v196, 16, v106
	v_and_b32_e32 v197, 0xffff0000, v106
	v_lshlrev_b32_e32 v102, 16, v107
	v_and_b32_e32 v103, 0xffff0000, v107
	v_lshlrev_b32_e32 v106, 16, v118
	v_and_b32_e32 v107, 0xffff0000, v118
	v_lshlrev_b32_e32 v118, 16, v119
	v_and_b32_e32 v119, 0xffff0000, v119
	v_lshlrev_b32_e32 v130, 16, v131
	v_and_b32_e32 v131, 0xffff0000, v131
	s_waitcnt vmcnt(24)
	v_lshlrev_b32_e32 v210, 16, v132
	v_and_b32_e32 v211, 0xffff0000, v132
	v_lshlrev_b32_e32 v132, 16, v133
	v_and_b32_e32 v133, 0xffff0000, v133
	s_waitcnt vmcnt(23)
	v_lshlrev_b32_e32 v218, 16, v134
	v_and_b32_e32 v219, 0xffff0000, v134
	v_lshlrev_b32_e32 v134, 16, v135
	v_and_b32_e32 v135, 0xffff0000, v135
	s_waitcnt vmcnt(22)
	v_lshlrev_b32_e32 v226, 16, v136
	v_and_b32_e32 v227, 0xffff0000, v136
	v_lshlrev_b32_e32 v136, 16, v137
	v_and_b32_e32 v137, 0xffff0000, v137
	s_waitcnt vmcnt(21)
	v_lshlrev_b32_e32 v234, 16, v138
	v_and_b32_e32 v235, 0xffff0000, v138
	v_lshlrev_b32_e32 v138, 16, v139
	v_and_b32_e32 v139, 0xffff0000, v139
	s_waitcnt vmcnt(20)
	v_lshlrev_b32_e32 v242, 16, v140
	v_and_b32_e32 v243, 0xffff0000, v140
	v_lshlrev_b32_e32 v140, 16, v141
	v_and_b32_e32 v141, 0xffff0000, v141
	v_pk_fma_f32 v[112:113], v[0:1], v[112:113], 0 op_sel_hi:[0,1,0]
	v_pk_fma_f32 v[200:201], v[0:1], v[208:209], 0 op_sel_hi:[0,1,0]
	v_pk_fma_f32 v[114:115], v[0:1], v[114:115], 0 op_sel_hi:[0,1,0]
	v_pk_fma_f32 v[202:203], v[0:1], v[216:217], 0 op_sel_hi:[0,1,0]
	v_pk_fma_f32 v[120:121], v[0:1], v[120:121], 0 op_sel_hi:[0,1,0]
	v_pk_fma_f32 v[208:209], v[0:1], v[224:225], 0 op_sel_hi:[0,1,0]
	v_pk_fma_f32 v[122:123], v[0:1], v[122:123], 0 op_sel_hi:[0,1,0]
	v_pk_fma_f32 v[216:217], v[0:1], v[232:233], 0 op_sel_hi:[0,1,0]
	v_pk_fma_f32 v[124:125], v[0:1], v[124:125], 0 op_sel_hi:[0,1,0]
	v_pk_fma_f32 v[224:225], v[0:1], v[240:241], 0 op_sel_hi:[0,1,0]
	v_pk_fma_f32 v[126:127], v[0:1], v[126:127], 0 op_sel_hi:[0,1,0]
	v_lshlrev_b32_e32 v198, 16, v108
	v_and_b32_e32 v199, 0xffff0000, v108
	v_lshlrev_b32_e32 v104, 16, v109
	v_and_b32_e32 v105, 0xffff0000, v109
	v_lshlrev_b32_e32 v108, 16, v128
	v_and_b32_e32 v109, 0xffff0000, v128
	v_lshlrev_b32_e32 v128, 16, v129
	v_and_b32_e32 v129, 0xffff0000, v129
	s_waitcnt vmcnt(19)
	v_lshlrev_b32_e32 v204, 16, v142
	v_and_b32_e32 v205, 0xffff0000, v142
	v_lshlrev_b32_e32 v142, 16, v143
	v_and_b32_e32 v143, 0xffff0000, v143
	s_waitcnt vmcnt(18)
	v_lshlrev_b32_e32 v212, 16, v144
	v_and_b32_e32 v213, 0xffff0000, v144
	v_lshlrev_b32_e32 v144, 16, v145
	v_and_b32_e32 v145, 0xffff0000, v145
	s_waitcnt vmcnt(17)
	v_lshlrev_b32_e32 v220, 16, v146
	v_and_b32_e32 v221, 0xffff0000, v146
	v_lshlrev_b32_e32 v146, 16, v147
	v_and_b32_e32 v147, 0xffff0000, v147
	s_waitcnt vmcnt(16)
	v_lshlrev_b32_e32 v228, 16, v148
	v_and_b32_e32 v229, 0xffff0000, v148
	v_lshlrev_b32_e32 v148, 16, v149
	v_and_b32_e32 v149, 0xffff0000, v149
	s_waitcnt vmcnt(15)
; __device__ __forceinline__ float bf_lo(unsigned w) { return __uint_as_float(w << 16); }
; __device__ __forceinline__ float bf_hi(unsigned w) { return __uint_as_float(w & 0xffff0000u); }
; __device__ __forceinline__ void p9_final(Frame& F) {
;     ...
;         for (int j = 0; j < 8; ++j) { f32x4 y = {0.f, 0.f, 0.f, 0.f};
; #pragma unroll
;             for (int k = 0; k < 4; ++k) { const float w = aw[k]; y[0] += w * bf_lo(q[k][j].x); y[1] += w * bf_hi(q[k][j].x); y[2] += w * bf_lo(q[k][j].y); y[3] += w * bf_hi(q[k][j].y); }
;             v[j] = x1[j] * DN_ALPHA + ((const f32x4*)(mod + (size_t)b * 12288 + 10240))[lane + 64 * j] * y; s += (v[j][0] + v[j][1]) + (v[j][2] + v[j][3]); }
	v_lshlrev_b32_e32 v236, 16, v150
	v_and_b32_e32 v237, 0xffff0000, v150
	v_lshlrev_b32_e32 v150, 16, v151
	v_and_b32_e32 v151, 0xffff0000, v151
	s_waitcnt vmcnt(14)
	v_lshlrev_b32_e32 v244, 16, v152
	v_and_b32_e32 v245, 0xffff0000, v152
	v_lshlrev_b32_e32 v152, 16, v153
	v_and_b32_e32 v153, 0xffff0000, v153
	v_pk_fma_f32 v[112:113], v[0:1], v[130:131], v[112:113] op_sel:[1,0,0]
	v_pk_fma_f32 v[130:131], v[0:1], v[210:211], v[200:201] op_sel:[1,0,0]
	v_pk_fma_f32 v[114:115], v[0:1], v[132:133], v[114:115] op_sel:[1,0,0]
	v_pk_fma_f32 v[132:133], v[0:1], v[218:219], v[202:203] op_sel:[1,0,0]
	v_pk_fma_f32 v[120:121], v[0:1], v[134:135], v[120:121] op_sel:[1,0,0]
	v_pk_fma_f32 v[134:135], v[0:1], v[226:227], v[208:209] op_sel:[1,0,0]
	v_pk_fma_f32 v[122:123], v[0:1], v[136:137], v[122:123] op_sel:[1,0,0]
	v_pk_fma_f32 v[136:137], v[0:1], v[234:235], v[216:217] op_sel:[1,0,0]
	v_pk_fma_f32 v[124:125], v[0:1], v[138:139], v[124:125] op_sel:[1,0,0]
	v_pk_fma_f32 v[138:139], v[0:1], v[242:243], v[224:225] op_sel:[1,0,0]
	v_pk_fma_f32 v[0:1], v[0:1], v[140:141], v[126:127] op_sel:[1,0,0]
	v_pk_fma_f32 v[126:127], v[2:3], v[196:197], v[248:249] op_sel_hi:[0,1,1]
	v_pk_fma_f32 v[102:103], v[2:3], v[102:103], v[250:251] op_sel_hi:[0,1,1]
	v_pk_fma_f32 v[106:107], v[2:3], v[106:107], v[252:253] op_sel_hi:[0,1,1]
	v_pk_fma_f32 v[110:111], v[2:3], v[118:119], v[110:111] op_sel_hi:[0,1,1]
	s_waitcnt vmcnt(13)
	v_lshlrev_b32_e32 v206, 16, v154
	v_and_b32_e32 v207, 0xffff0000, v154
	v_lshlrev_b32_e32 v154, 16, v155
	v_and_b32_e32 v155, 0xffff0000, v155
	s_waitcnt vmcnt(12)
	v_lshlrev_b32_e32 v214, 16, v156
	v_and_b32_e32 v215, 0xffff0000, v156
	v_lshlrev_b32_e32 v156, 16, v157
	v_and_b32_e32 v157, 0xffff0000, v157
	s_waitcnt vmcnt(11)
	v_lshlrev_b32_e32 v222, 16, v158
	v_and_b32_e32 v223, 0xffff0000, v158
	v_lshlrev_b32_e32 v158, 16, v159
	v_and_b32_e32 v159, 0xffff0000, v159
	s_waitcnt vmcnt(10)
	v_lshlrev_b32_e32 v230, 16, v160
	v_and_b32_e32 v231, 0xffff0000, v160
	v_lshlrev_b32_e32 v160, 16, v161
	v_and_b32_e32 v161, 0xffff0000, v161
	s_waitcnt vmcnt(9)
	v_lshlrev_b32_e32 v238, 16, v162
	v_and_b32_e32 v239, 0xffff0000, v162
	v_lshlrev_b32_e32 v162, 16, v163
	v_and_b32_e32 v163, 0xffff0000, v163
	s_waitcnt vmcnt(8)
	v_lshlrev_b32_e32 v246, 16, v164
	v_and_b32_e32 v247, 0xffff0000, v164
	v_lshlrev_b32_e32 v164, 16, v165
	v_and_b32_e32 v165, 0xffff0000, v165
	v_pk_fma_f32 v[116:117], v[2:3], v[204:205], v[116:117] op_sel_hi:[0,1,1]
	v_pk_fma_f32 v[112:113], v[2:3], v[142:143], v[112:113] op_sel_hi:[0,1,1]
	v_pk_fma_f32 v[118:119], v[2:3], v[212:213], v[130:131] op_sel_hi:[0,1,1]
	v_pk_fma_f32 v[114:115], v[2:3], v[144:145], v[114:115] op_sel_hi:[0,1,1]
	v_pk_fma_f32 v[130:131], v[2:3], v[220:221], v[132:133] op_sel_hi:[0,1,1]
	v_pk_fma_f32 v[120:121], v[2:3], v[146:147], v[120:121] op_sel_hi:[0,1,1]
	v_pk_fma_f32 v[132:133], v[2:3], v[228:229], v[134:135] op_sel_hi:[0,1,1]
	v_pk_fma_f32 v[122:123], v[2:3], v[148:149], v[122:123] op_sel_hi:[0,1,1]
	v_pk_fma_f32 v[134:135], v[2:3], v[236:237], v[136:137] op_sel_hi:[0,1,1]
	v_pk_fma_f32 v[124:125], v[2:3], v[150:151], v[124:125] op_sel_hi:[0,1,1]
	v_pk_fma_f32 v[136:137], v[2:3], v[244:245], v[138:139] op_sel_hi:[0,1,1]
	v_pk_fma_f32 v[0:1], v[2:3], v[152:153], v[0:1] op_sel_hi:[0,1,1]
	v_pk_fma_f32 v[2:3], v[24:25], v[198:199], v[126:127] op_sel_hi:[0,1,1]
	v_pk_fma_f32 v[102:103], v[24:25], v[104:105], v[102:103] op_sel_hi:[0,1,1]
	v_pk_fma_f32 v[104:105], v[24:25], v[108:109], v[106:107] op_sel_hi:[0,1,1]
	v_pk_fma_f32 v[106:107], v[24:25], v[128:129], v[110:111] op_sel_hi:[0,1,1]
	v_pk_fma_f32 v[108:109], v[24:25], v[206:207], v[116:117] op_sel_hi:[0,1,1]
	v_pk_fma_f32 v[110:111], v[24:25], v[154:155], v[112:113] op_sel_hi:[0,1,1]
	v_pk_fma_f32 v[112:113], v[24:25], v[214:215], v[118:119] op_sel_hi:[0,1,1]
	v_pk_fma_f32 v[114:115], v[24:25], v[156:157], v[114:115] op_sel_hi:[0,1,1]
	v_pk_fma_f32 v[116:117], v[24:25], v[222:223], v[130:131] op_sel_hi:[0,1,1]
	v_pk_fma_f32 v[118:119], v[24:25], v[158:159], v[120:121] op_sel_hi:[0,1,1]
	v_pk_fma_f32 v[122:123], v[24:25], v[160:161], v[122:123] op_sel_hi:[0,1,1]
	v_pk_fma_f32 v[124:125], v[24:25], v[162:163], v[124:125] op_sel_hi:[0,1,1]
	v_pk_fma_f32 v[0:1], v[24:25], v[164:165], v[0:1] op_sel_hi:[0,1,1]
	s_waitcnt vmcnt(7)
	v_pk_mul_f32 v[2:3], v[2:3], v[82:83]
	v_pk_mul_f32 v[82:83], v[102:103], v[84:85]
	s_waitcnt vmcnt(6)
	v_pk_mul_f32 v[84:85], v[104:105], v[86:87]
	v_pk_mul_f32 v[86:87], v[106:107], v[88:89]
	v_pk_fma_f32 v[126:127], v[24:25], v[238:239], v[134:135] op_sel_hi:[0,1,1]
	v_pk_fma_f32 v[128:129], v[24:25], v[246:247], v[136:137] op_sel_hi:[0,1,1]
	s_waitcnt vmcnt(5)
	v_pk_mul_f32 v[88:89], v[108:109], v[90:91]
	v_pk_mul_f32 v[90:91], v[110:111], v[92:93]
	s_waitcnt vmcnt(4)
	v_pk_mul_f32 v[92:93], v[112:113], v[94:95]
	v_pk_mul_f32 v[94:95], v[114:115], v[96:97]
	s_waitcnt vmcnt(3)
	v_pk_mul_f32 v[96:97], v[116:117], v[98:99]
	v_pk_mul_f32 v[98:99], v[118:119], v[100:101]
	s_waitcnt vmcnt(2)
	v_pk_mul_f32 v[52:53], v[122:123], v[52:53]
	s_waitcnt vmcnt(1)
	v_pk_mul_f32 v[102:103], v[124:125], v[56:57]
	s_waitcnt vmcnt(0)
; __device__ __forceinline__ void p9_final(Frame& F) {
;     ...
;             v[j] = x1[j] * DN_ALPHA + ((const f32x4*)(mod + (size_t)b * 12288 + 10240))[lane + 64 * j] * y; s += (v[j][0] + v[j][1]) + (v[j][2] + v[j][3]); }
;         const float mean = wave_sum(s) * (1.f / DM); float s2 = 0.f;
; #pragma unroll
;         for (int j = 0; j < 8; ++j) { v[j] = v[j] - mean; s2 += (v[j][0] * v[j][0] + v[j][1] * v[j][1]) + (v[j][2] * v[j][2] + v[j][3] * v[j][3]); }
;         const float rstd = 1.f / sqrtf(wave_sum(s2) * (1.f / DM) + LN_EPS);
; #pragma unroll
;         for (int j = 0; j < 8; ++j) __builtin_nontemporal_store(v[j] * rstd * ((const f32x4*)F.in[I_LN2W])[lane + 64 * j] + ((const f32x4*)F.in[I_LN2B])[lane + 64 * j], (f32x4*)(F.out + (size_t)t * DM) + lane + 64 * j);
	global_load_dwordx4 v[160:163], v[26:27], off offset:1024
	global_load_dwordx4 v[196:199], v[28:29], off offset:1024
	global_load_dwordx4 v[200:203], v[26:27], off offset:2048
	global_load_dwordx4 v[204:207], v[28:29], off offset:2048
	global_load_dwordx4 v[208:211], v[26:27], off offset:3072
	global_load_dwordx4 v[212:215], v[28:29], off offset:3072
	global_load_dwordx4 v[216:219], v[30:31], off
	global_load_dwordx4 v[220:223], v[32:33], off
	global_load_dwordx4 v[224:227], v[34:35], off
	global_load_dwordx4 v[232:235], v[36:37], off
	global_load_dwordx4 v[236:239], v[38:39], off
	global_load_dwordx4 v[240:243], v[40:41], off
	global_load_dwordx4 v[244:247], v[42:43], off
	global_load_dwordx4 v[248:251], v[44:45], off
	v_pk_mul_f32 v[106:107], v[0:1], v[60:61]
	v_pk_fma_f32 v[82:83], v[168:169], s[12:13], v[82:83] op_sel_hi:[1,0,1]
	v_pk_fma_f32 v[108:109], v[166:167], s[12:13], v[2:3] op_sel_hi:[1,0,1]
	v_pk_fma_f32 v[86:87], v[174:175], s[12:13], v[86:87] op_sel_hi:[1,0,1]
	v_pk_fma_f32 v[84:85], v[172:173], s[12:13], v[84:85] op_sel_hi:[1,0,1]
	v_pk_mul_f32 v[100:101], v[126:127], v[54:55]
	v_pk_mul_f32 v[104:105], v[128:129], v[58:59]
	v_pk_fma_f32 v[90:91], v[178:179], s[12:13], v[90:91] op_sel_hi:[1,0,1]
	v_pk_fma_f32 v[88:89], v[176:177], s[12:13], v[88:89] op_sel_hi:[1,0,1]
	v_pk_fma_f32 v[60:61], v[186:187], s[12:13], v[98:99] op_sel_hi:[1,0,1]
	v_pk_fma_f32 v[58:59], v[184:185], s[12:13], v[96:97] op_sel_hi:[1,0,1]
	v_pk_fma_f32 v[56:57], v[190:191], s[12:13], v[52:53] op_sel_hi:[1,0,1]
	v_pk_fma_f32 v[2:3], v[62:63], s[12:13], v[102:103] op_sel_hi:[1,0,1]
	v_pk_fma_f32 v[52:53], v[64:65], s[12:13], v[106:107] op_sel_hi:[1,0,1]
	v_mov_b32_e32 v62, v108
	v_mov_b32_e32 v63, v84
	v_mov_b32_e32 v64, v109
	v_mov_b32_e32 v65, v85
	v_mov_b32_e32 v96, v82
	v_mov_b32_e32 v97, v86
	v_mov_b32_e32 v98, v83
	v_mov_b32_e32 v99, v87
	v_pk_fma_f32 v[0:1], v[192:193], s[12:13], v[100:101] op_sel_hi:[1,0,1]
	v_pk_mov_b32 v[100:101], v[88:89], v[90:91] op_sel:[1,0]
	v_mov_b32_e32 v102, v88
	v_mov_b32_e32 v103, v91
	v_pk_add_f32 v[62:63], v[62:63], v[64:65]
	v_pk_add_f32 v[64:65], v[96:97], v[98:99]
	v_pk_fma_f32 v[120:121], v[24:25], v[230:231], v[132:133] op_sel_hi:[0,1,1]
	v_pk_add_f32 v[96:97], v[100:101], v[102:103]
	v_pk_add_f32 v[62:63], v[62:63], v[64:65]
	v_pk_mul_f32 v[50:51], v[120:121], v[50:51]
	v_pk_fma_f32 v[94:95], v[182:183], s[12:13], v[94:95] op_sel_hi:[1,0,1]
	v_pk_fma_f32 v[92:93], v[180:181], s[12:13], v[92:93] op_sel_hi:[1,0,1]
	v_pk_add_f32 v[64:65], v[96:97], v[96:97] op_sel:[0,1] op_sel_hi:[1,0]
	v_add_f32_e32 v24, 0, v62
	v_pk_fma_f32 v[54:55], v[188:189], s[12:13], v[50:51] op_sel_hi:[1,0,1]
	v_pk_fma_f32 v[50:51], v[194:195], s[12:13], v[104:105] op_sel_hi:[1,0,1]
	v_add_f32_e32 v104, v92, v93
	v_add_f32_e32 v106, v94, v95
	v_mov_b32_e32 v111, v58
	v_mov_b32_e32 v105, v60
	v_mov_b32_e32 v107, v61
	v_mov_b32_e32 v65, v59
	v_add_f32_e32 v110, v24, v63
	v_pk_mov_b32 v[112:113], v[54:55], v[56:57] op_sel:[1,0]
	v_mov_b32_e32 v114, v54
	v_mov_b32_e32 v115, v57
	v_pk_add_f32 v[98:99], v[104:105], v[106:107]
	v_pk_add_f32 v[62:63], v[110:111], v[64:65]
	v_pk_add_f32 v[100:101], v[112:113], v[114:115]
	v_pk_add_f32 v[62:63], v[62:63], v[98:99]
	v_pk_add_f32 v[96:97], v[100:101], v[100:101] op_sel:[0,1] op_sel_hi:[1,0]
	v_pk_add_f32 v[62:63], v[62:63], v[62:63] op_sel:[0,1] op_sel_hi:[1,0]
	v_add_f32_e32 v116, v0, v1
	v_add_f32_e32 v118, v2, v3
	v_mov_b32_e32 v117, v52
	v_mov_b32_e32 v119, v53
	v_mov_b32_e32 v97, v51
	v_mov_b32_e32 v63, v50
	v_pk_add_f32 v[102:103], v[116:117], v[118:119]
	v_pk_add_f32 v[62:63], v[62:63], v[96:97]
	v_readfirstlane_b32 s2, v10
	v_pk_add_f32 v[62:63], v[62:63], v[102:103]
	v_readfirstlane_b32 s3, v11
	v_add_f32_e32 v24, v62, v63
	ds_bpermute_b32 v62, v66, v24
	s_waitcnt lgkmcnt(0)
	v_add_f32_e32 v24, v24, v62
	ds_bpermute_b32 v62, v67, v24
	s_waitcnt lgkmcnt(0)
	v_add_f32_e32 v24, v24, v62
	ds_bpermute_b32 v62, v68, v24
	s_waitcnt lgkmcnt(0)
	v_add_f32_e32 v24, v24, v62
	ds_bpermute_b32 v62, v69, v24
	s_waitcnt lgkmcnt(0)
	v_add_f32_e32 v24, v24, v62
	ds_bpermute_b32 v62, v70, v24
	s_waitcnt lgkmcnt(0)
	v_add_f32_e32 v24, v24, v62
	ds_bpermute_b32 v62, v71, v24
	s_waitcnt lgkmcnt(0)
	v_add_f32_e32 v24, v24, v62
	v_fmamk_f32 v83, v24, 0xba000000, v83
	v_fmamk_f32 v109, v24, 0xba000000, v109
	v_fmamk_f32 v87, v24, 0xba000000, v87
	v_fmamk_f32 v85, v24, 0xba000000, v85
	v_fmac_f32_e32 v82, 0xba000000, v24
	v_fmac_f32_e32 v108, 0xba000000, v24
	v_fmac_f32_e32 v86, 0xba000000, v24
	v_fmac_f32_e32 v84, 0xba000000, v24
	v_fmamk_f32 v89, v24, 0xba000000, v89
	v_fmac_f32_e32 v88, 0xba000000, v24
	v_fmamk_f32 v91, v24, 0xba000000, v91
	v_fmac_f32_e32 v90, 0xba000000, v24
	v_mov_b32_e32 v64, v109
	v_mov_b32_e32 v65, v85
	v_mov_b32_e32 v98, v83
	v_mov_b32_e32 v99, v87
	v_mov_b32_e32 v62, v108
	v_mov_b32_e32 v63, v84
	v_mov_b32_e32 v96, v82
	v_mov_b32_e32 v97, v86
	v_pk_mul_f32 v[100:101], v[90:91], v[90:91]
	v_pk_mul_f32 v[102:103], v[88:89], v[88:89]
	v_pk_mul_f32 v[64:65], v[64:65], v[64:65]
	v_pk_mul_f32 v[98:99], v[98:99], v[98:99]
	v_fmac_f32_e32 v92, 0xba000000, v24
	v_fmac_f32_e32 v94, 0xba000000, v24
	v_pk_mov_b32 v[116:117], v[102:103], v[100:101] op_sel:[1,0]
	v_mov_b32_e32 v103, v101
	v_pk_fma_f32 v[62:63], v[62:63], v[62:63], v[64:65]
	v_pk_fma_f32 v[64:65], v[96:97], v[96:97], v[98:99]
	v_fmamk_f32 v93, v24, 0xba000000, v93
	v_fmamk_f32 v95, v24, 0xba000000, v95
	v_fmamk_f32 v61, v24, 0xba000000, v61
	v_fmac_f32_e32 v60, 0xba000000, v24
	v_fmamk_f32 v59, v24, 0xba000000, v59
	v_fmac_f32_e32 v58, 0xba000000, v24
	v_fmamk_f32 v55, v24, 0xba000000, v55
	v_fmac_f32_e32 v54, 0xba000000, v24
; __device__ __forceinline__ void p9_final(Frame& F) {
;     ...
;         const float mean = wave_sum(s) * (1.f / DM); float s2 = 0.f;
; #pragma unroll
;         for (int j = 0; j < 8; ++j) { v[j] = v[j] - mean; s2 += (v[j][0] * v[j][0] + v[j][1] * v[j][1]) + (v[j][2] * v[j][2] + v[j][3] * v[j][3]); }
;         const float rstd = 1.f / sqrtf(wave_sum(s2) * (1.f / DM) + LN_EPS);
; #pragma unroll
;         for (int j = 0; j < 8; ++j) __builtin_nontemporal_store(v[j] * rstd * ((const f32x4*)F.in[I_LN2W])[lane + 64 * j] + ((const f32x4*)F.in[I_LN2B])[lane + 64 * j], (f32x4*)(F.out + (size_t)t * DM) + lane + 64 * j);
	v_fmamk_f32 v57, v24, 0xba000000, v57
	v_fmac_f32_e32 v56, 0xba000000, v24
	v_fmamk_f32 v1, v24, 0xba000000, v1
	v_fmac_f32_e32 v0, 0xba000000, v24
	v_fmamk_f32 v3, v24, 0xba000000, v3
	v_fmac_f32_e32 v2, 0xba000000, v24
	v_fmamk_f32 v53, v24, 0xba000000, v53
	v_fmac_f32_e32 v52, 0xba000000, v24
	v_fmamk_f32 v51, v24, 0xba000000, v51
	v_fmac_f32_e32 v50, 0xba000000, v24
	v_mul_f32_e32 v24, v92, v92
	v_mul_f32_e32 v104, v94, v94
	v_pk_add_f32 v[96:97], v[116:117], v[102:103]
	v_pk_add_f32 v[62:63], v[62:63], v[64:65]
	v_pk_fma_f32 v[100:101], v[92:93], v[92:93], v[24:25] op_sel_hi:[1,1,0]
	v_pk_fma_f32 v[104:105], v[94:95], v[94:95], v[104:105] op_sel_hi:[1,1,0]
	v_pk_add_f32 v[64:65], v[96:97], v[96:97] op_sel_hi:[0,1]
	v_pk_add_f32 v[62:63], v[62:63], v[62:63] op_sel_hi:[0,1]
	v_pk_mul_f32 v[106:107], v[56:57], v[56:57]
	v_pk_mul_f32 v[110:111], v[54:55], v[54:55]
	v_mul_f32_e32 v100, v58, v58
	v_mul_f32_e32 v104, v59, v59
	v_mul_f32_e32 v64, v60, v60
	v_mul_f32_e32 v62, v61, v61
	v_pk_mov_b32 v[118:119], v[110:111], v[106:107] op_sel:[1,0]
	v_mov_b32_e32 v111, v107
	v_pk_add_f32 v[96:97], v[100:101], v[104:105]
	v_pk_add_f32 v[62:63], v[64:65], v[62:63]
	v_mul_f32_e32 v112, v0, v0
	v_mul_f32_e32 v114, v2, v2
	v_pk_add_f32 v[98:99], v[118:119], v[110:111]
	v_pk_add_f32 v[62:63], v[96:97], v[62:63]
	v_pk_fma_f32 v[106:107], v[0:1], v[0:1], v[112:113] op_sel_hi:[1,1,0]
	v_pk_fma_f32 v[112:113], v[2:3], v[2:3], v[114:115] op_sel_hi:[1,1,0]
	v_pk_add_f32 v[98:99], v[98:99], v[98:99] op_sel_hi:[0,1]
	v_pk_add_f32 v[62:63], v[62:63], v[62:63] op_sel_hi:[0,1]
	v_mul_f32_e32 v106, v50, v50
	v_mul_f32_e32 v112, v51, v51
	v_mul_f32_e32 v98, v52, v52
	v_mul_f32_e32 v62, v53, v53
	v_pk_add_f32 v[100:101], v[106:107], v[112:113]
	v_pk_add_f32 v[62:63], v[98:99], v[62:63]
	s_nop 0
	v_pk_add_f32 v[62:63], v[100:101], v[62:63]
	s_nop 0
	v_add_f32_e32 v24, v62, v63
	ds_bpermute_b32 v62, v66, v24
	s_waitcnt lgkmcnt(0)
	v_add_f32_e32 v24, v24, v62
	ds_bpermute_b32 v62, v67, v24
	s_waitcnt lgkmcnt(0)
	v_add_f32_e32 v24, v24, v62
	ds_bpermute_b32 v62, v68, v24
	s_waitcnt lgkmcnt(0)
	v_add_f32_e32 v24, v24, v62
	ds_bpermute_b32 v62, v69, v24
	s_waitcnt lgkmcnt(0)
	v_add_f32_e32 v24, v24, v62
	ds_bpermute_b32 v62, v70, v24
	s_waitcnt lgkmcnt(0)
	v_add_f32_e32 v24, v24, v62
	ds_bpermute_b32 v62, v71, v24
	s_waitcnt lgkmcnt(0)
	v_add_f32_e32 v24, v24, v62
	v_fmamk_f32 v24, v24, 0x3a000000, v79
	v_mul_f32_e32 v62, 0x4f800000, v24
	v_cmp_gt_f32_e32 vcc, s15, v24
	s_nop 1
	v_cndmask_b32_e32 v24, v24, v62, vcc
	v_sqrt_f32_e32 v62, v24
	s_nop 0
	v_add_u32_e32 v63, -1, v62
	v_add_u32_e32 v64, 1, v62
	v_fma_f32 v65, -v63, v62, v24
	v_fma_f32 v81, -v64, v62, v24
	v_cmp_ge_f32_e64 s[0:1], 0, v65
	s_nop 1
	v_cndmask_b32_e64 v62, v62, v63, s[0:1]
	v_cmp_lt_f32_e64 s[0:1], 0, v81
	s_nop 1
	v_cndmask_b32_e64 v62, v62, v64, s[0:1]
	v_mul_f32_e32 v63, 0x37800000, v62
	v_cndmask_b32_e32 v62, v62, v63, vcc
	v_cmp_class_f32_e32 vcc, v24, v80
	s_nop 1
	v_cndmask_b32_e32 v24, v62, v24, vcc
	v_div_scale_f32 v62, s[0:1], v24, v24, 1.0
	v_rcp_f32_e32 v64, v62
	v_div_scale_f32 v63, vcc, 1.0, v24, 1.0
	v_readfirstlane_b32 s0, v8
	v_fma_f32 v65, -v62, v64, 1.0
	v_fmac_f32_e32 v64, v65, v64
	v_mul_f32_e32 v65, v63, v64
	v_fma_f32 v81, -v62, v65, v63
	v_fmac_f32_e32 v65, v81, v64
	v_fma_f32 v62, -v62, v65, v63
	v_div_fmas_f32 v62, v62, v64, v65
	v_div_fixup_f32 v24, v62, v24, 1.0
	v_pk_mul_f32 v[62:63], v[108:109], v[24:25] op_sel_hi:[1,0]
	v_pk_mul_f32 v[64:65], v[82:83], v[24:25] op_sel_hi:[1,0]
	v_pk_fma_f32 v[16:17], v[16:17], v[62:63], v[20:21]
	v_pk_fma_f32 v[18:19], v[18:19], v[64:65], v[22:23]
	global_store_dwordx4 v[46:47], v[16:19], off offset:-4096 nt
	s_nop 1
	v_pk_mul_f32 v[62:63], v[86:87], v[24:25] op_sel_hi:[1,0]
	v_pk_mul_f32 v[64:65], v[84:85], v[24:25] op_sel_hi:[1,0]
	v_pk_mul_f32 v[60:61], v[60:61], v[24:25] op_sel_hi:[1,0]
	v_pk_mul_f32 v[58:59], v[58:59], v[24:25] op_sel_hi:[1,0]
	v_pk_mul_f32 v[56:57], v[56:57], v[24:25] op_sel_hi:[1,0]
	v_pk_mul_f32 v[54:55], v[54:55], v[24:25] op_sel_hi:[1,0]
	v_pk_mul_f32 v[2:3], v[2:3], v[24:25] op_sel_hi:[1,0]
	v_pk_mul_f32 v[0:1], v[0:1], v[24:25] op_sel_hi:[1,0]
	v_readfirstlane_b32 s1, v9
	v_pk_mul_f32 v[10:11], v[52:53], v[24:25] op_sel_hi:[1,0]
	v_pk_mul_f32 v[8:9], v[50:51], v[24:25] op_sel_hi:[1,0]
	s_and_b64 vcc, s[24:25], exec
	s_waitcnt vmcnt(13)
	v_pk_fma_f32 v[16:17], v[160:161], v[64:65], v[196:197]
	v_pk_fma_f32 v[18:19], v[162:163], v[62:63], v[198:199]
	global_store_dwordx4 v[46:47], v[16:19], off offset:-3072 nt
	s_nop 1
	v_pk_mul_f32 v[62:63], v[90:91], v[24:25] op_sel_hi:[1,0]
	v_pk_mul_f32 v[64:65], v[88:89], v[24:25] op_sel_hi:[1,0]
	s_waitcnt vmcnt(12)
	v_pk_fma_f32 v[18:19], v[202:203], v[62:63], v[206:207]
	v_pk_fma_f32 v[16:17], v[200:201], v[64:65], v[204:205]
	global_store_dwordx4 v[46:47], v[16:19], off offset:-2048 nt
	s_nop 1
	v_pk_mul_f32 v[62:63], v[94:95], v[24:25] op_sel_hi:[1,0]
	v_pk_mul_f32 v[64:65], v[92:93], v[24:25] op_sel_hi:[1,0]
	s_waitcnt vmcnt(11)
	v_pk_fma_f32 v[18:19], v[210:211], v[62:63], v[214:215]
	v_pk_fma_f32 v[16:17], v[208:209], v[64:65], v[212:213]
	global_store_dwordx4 v[46:47], v[16:19], off offset:-1024 nt
	s_nop 1
	s_waitcnt vmcnt(10)
	v_pk_fma_f32 v[16:17], v[216:217], v[58:59], v[220:221]
	v_pk_fma_f32 v[18:19], v[218:219], v[60:61], v[222:223]
	global_store_dwordx4 v[46:47], v[16:19], off nt
	s_nop 1
	s_waitcnt vmcnt(9)
	v_pk_fma_f32 v[16:17], v[54:55], v[224:225], v[232:233]
	v_pk_fma_f32 v[18:19], v[56:57], v[226:227], v[234:235]
	global_store_dwordx4 v[46:47], v[16:19], off offset:1024 nt
	s_nop 1
	s_waitcnt vmcnt(8)
	v_pk_fma_f32 v[0:1], v[0:1], v[236:237], v[240:241]
	v_pk_fma_f32 v[2:3], v[2:3], v[238:239], v[242:243]
	global_store_dwordx4 v[46:47], v[0:3], off offset:2048 nt
	s_nop 1
	v_mov_b64_e32 v[0:1], v[12:13]
	v_mov_b64_e32 v[2:3], v[14:15]
	s_waitcnt vmcnt(7)
	v_pk_fma_f32 v[8:9], v[8:9], v[244:245], v[248:249]
	v_pk_fma_f32 v[10:11], v[10:11], v[246:247], v[250:251]
	global_store_dwordx4 v[46:47], v[8:11], off offset:3072 nt
	v_lshl_add_u64 v[46:47], v[46:47], 0, s[8:9]
	s_cbranch_vccnz .LBB0_1211
